# out-projection GEMM set-up: full vmcnt wait before each tile's K-loop became a counted wait (the epilogue already retired the staged tiles), so the last output stores drain under the first K phases
# baseline (speedup 1.0000x reference)
.LBB0_1047:
	s_ashr_i32 s45, s44, 31
	s_lshl_b64 s[46:47], s[44:45], 20
	v_readlane_b32 s9, v253, 62
	s_add_u32 s46, s9, s46
	v_readlane_b32 s9, v253, 63
	s_addc_u32 s47, s9, s47
	s_and_b64 s[48:49], s[40:41], exec
	s_cselect_b32 s45, s47, s11
	s_cselect_b32 s88, s46, s10
	s_ashr_i32 s9, s8, 31
	s_lshl_b64 s[48:49], s[8:9], 20
	s_add_u32 s48, s12, s48
	s_addc_u32 s49, s13, s49
	s_and_b64 s[52:53], s[40:41], exec
	s_cselect_b32 s9, s49, s51
	s_cselect_b32 s90, s48, s50
	s_add_u32 s10, s10, 0x80080
	s_addc_u32 s11, s11, 0
	s_add_u32 s91, s50, 0x100
	v_mov_b32_e32 v2, 0
	s_waitcnt lgkmcnt(0)
	s_addc_u32 s92, s51, 0
	s_mov_b32 s93, -2
	v_mov_b32_e32 v3, v2
	v_mov_b32_e32 v4, v2
	v_mov_b32_e32 v5, v2
	v_mov_b32_e32 v6, v2
	v_mov_b32_e32 v7, v2
	v_mov_b32_e32 v8, v2
	v_mov_b32_e32 v9, v2
	v_mov_b32_e32 v18, v2
	v_mov_b32_e32 v19, v2
	v_mov_b32_e32 v20, v2
	v_mov_b32_e32 v21, v2
	v_mov_b32_e32 v22, v2
	v_mov_b32_e32 v23, v2
	v_mov_b32_e32 v24, v2
	v_mov_b32_e32 v25, v2
	v_mov_b32_e32 v34, v2
	v_mov_b32_e32 v35, v2
	v_mov_b32_e32 v36, v2
	v_mov_b32_e32 v37, v2
	v_mov_b32_e32 v38, v2
	v_mov_b32_e32 v39, v2
	v_mov_b32_e32 v40, v2
	v_mov_b32_e32 v41, v2
	v_mov_b32_e32 v66, v2
	v_mov_b32_e32 v67, v2
	v_mov_b32_e32 v68, v2
	v_mov_b32_e32 v69, v2
	v_mov_b32_e32 v70, v2
	v_mov_b32_e32 v71, v2
	v_mov_b32_e32 v72, v2
	v_mov_b32_e32 v73, v2
	v_mov_b32_e32 v10, v2
	v_mov_b32_e32 v11, v2
	v_mov_b32_e32 v12, v2
	v_mov_b32_e32 v13, v2
	v_mov_b32_e32 v14, v2
	v_mov_b32_e32 v15, v2
	v_mov_b32_e32 v16, v2
	v_mov_b32_e32 v17, v2
	v_mov_b32_e32 v26, v2
	v_mov_b32_e32 v27, v2
	v_mov_b32_e32 v28, v2
	v_mov_b32_e32 v29, v2
	v_mov_b32_e32 v30, v2
	v_mov_b32_e32 v31, v2
	v_mov_b32_e32 v32, v2
	v_mov_b32_e32 v33, v2
	v_mov_b32_e32 v50, v2
	v_mov_b32_e32 v51, v2
	v_mov_b32_e32 v52, v2
	v_mov_b32_e32 v53, v2
	v_mov_b32_e32 v54, v2
	v_mov_b32_e32 v55, v2
	v_mov_b32_e32 v56, v2
	v_mov_b32_e32 v57, v2
	v_mov_b32_e32 v74, v2
	v_mov_b32_e32 v75, v2
	v_mov_b32_e32 v76, v2
	v_mov_b32_e32 v77, v2
	v_mov_b32_e32 v78, v2
	v_mov_b32_e32 v79, v2
	v_mov_b32_e32 v80, v2
	v_mov_b32_e32 v81, v2
	v_mov_b32_e32 v82, v2
	v_mov_b32_e32 v83, v2
	v_mov_b32_e32 v84, v2
	v_mov_b32_e32 v85, v2
	v_mov_b32_e32 v86, v2
	v_mov_b32_e32 v87, v2
	v_mov_b32_e32 v88, v2
	v_mov_b32_e32 v89, v2
	v_mov_b32_e32 v100, v2
	v_mov_b32_e32 v101, v2
	v_mov_b32_e32 v102, v2
	v_mov_b32_e32 v103, v2
	v_mov_b32_e32 v104, v2
	v_mov_b32_e32 v105, v2
	v_mov_b32_e32 v106, v2
	v_mov_b32_e32 v107, v2
	v_mov_b32_e32 v116, v2
	v_mov_b32_e32 v117, v2
	v_mov_b32_e32 v118, v2
	v_mov_b32_e32 v119, v2
	v_mov_b32_e32 v120, v2
	v_mov_b32_e32 v121, v2
	v_mov_b32_e32 v122, v2
	v_mov_b32_e32 v123, v2
	v_mov_b32_e32 v132, v2
	v_mov_b32_e32 v133, v2
	v_mov_b32_e32 v134, v2
	v_mov_b32_e32 v135, v2
	v_mov_b32_e32 v136, v2
	v_mov_b32_e32 v137, v2
	v_mov_b32_e32 v138, v2
	v_mov_b32_e32 v139, v2
	v_mov_b32_e32 v90, v2
	v_mov_b32_e32 v91, v2
	v_mov_b32_e32 v92, v2
	v_mov_b32_e32 v93, v2
	v_mov_b32_e32 v94, v2
	v_mov_b32_e32 v95, v2
	v_mov_b32_e32 v96, v2
	v_mov_b32_e32 v97, v2
	v_mov_b32_e32 v108, v2
	v_mov_b32_e32 v109, v2
	v_mov_b32_e32 v110, v2
	v_mov_b32_e32 v111, v2
	v_mov_b32_e32 v112, v2
	v_mov_b32_e32 v113, v2
	v_mov_b32_e32 v114, v2
	v_mov_b32_e32 v115, v2
	v_mov_b32_e32 v124, v2
	v_mov_b32_e32 v125, v2
	v_mov_b32_e32 v126, v2
	v_mov_b32_e32 v127, v2
	v_mov_b32_e32 v128, v2
	v_mov_b32_e32 v129, v2
	v_mov_b32_e32 v130, v2
	v_mov_b32_e32 v131, v2
	v_mov_b32_e32 v140, v2
	v_mov_b32_e32 v141, v2
	v_mov_b32_e32 v142, v2
	v_mov_b32_e32 v143, v2
	v_mov_b32_e32 v144, v2
	v_mov_b32_e32 v145, v2
	v_mov_b32_e32 v146, v2
	v_mov_b32_e32 v147, v2
	s_waitcnt vmcnt(8)

.LBB0_1067:
	s_ashr_i32 s49, s48, 31
	s_lshl_b64 s[50:51], s[48:49], 20
	v_readlane_b32 s31, v253, 62
	s_add_u32 s50, s31, s50
	v_readlane_b32 s31, v253, 63
	s_addc_u32 s51, s31, s51
	s_and_b64 s[52:53], s[40:41], exec
	s_cselect_b32 s49, s51, s11
	s_cselect_b32 s93, s50, s10
	s_ashr_i32 s47, s46, 31
	s_lshl_b64 s[52:53], s[46:47], 20
	s_add_u32 s52, s12, s52
	s_addc_u32 s53, s13, s53
	s_and_b64 s[56:57], s[40:41], exec
	s_cselect_b32 s47, s53, s55
	s_cselect_b32 s94, s52, s54
	s_add_u32 s10, s10, 0x80080
	s_addc_u32 s11, s11, 0
	s_add_u32 s95, s54, 0x100
	v_mov_b32_e32 v2, 0
	s_addc_u32 s96, s55, 0
	s_mov_b32 s97, -2
	v_mov_b32_e32 v3, v2
	v_mov_b32_e32 v4, v2
	v_mov_b32_e32 v5, v2
	v_mov_b32_e32 v6, v2
	v_mov_b32_e32 v7, v2
	v_mov_b32_e32 v8, v2
	v_mov_b32_e32 v9, v2
	v_mov_b32_e32 v18, v2
	v_mov_b32_e32 v19, v2
	v_mov_b32_e32 v20, v2
	v_mov_b32_e32 v21, v2
	v_mov_b32_e32 v22, v2
	v_mov_b32_e32 v23, v2
	v_mov_b32_e32 v24, v2
	v_mov_b32_e32 v25, v2
	v_mov_b32_e32 v34, v2
	v_mov_b32_e32 v35, v2
	v_mov_b32_e32 v36, v2
	v_mov_b32_e32 v37, v2
	v_mov_b32_e32 v38, v2
	v_mov_b32_e32 v39, v2
	v_mov_b32_e32 v40, v2
	v_mov_b32_e32 v41, v2
	v_mov_b32_e32 v58, v2
	v_mov_b32_e32 v59, v2
	v_mov_b32_e32 v60, v2
	v_mov_b32_e32 v61, v2
	v_mov_b32_e32 v62, v2
	v_mov_b32_e32 v63, v2
	v_mov_b32_e32 v64, v2
	v_mov_b32_e32 v65, v2
	v_mov_b32_e32 v10, v2
	v_mov_b32_e32 v11, v2
	v_mov_b32_e32 v12, v2
	v_mov_b32_e32 v13, v2
	v_mov_b32_e32 v14, v2
	v_mov_b32_e32 v15, v2
	v_mov_b32_e32 v16, v2
	v_mov_b32_e32 v17, v2
	v_mov_b32_e32 v26, v2
	v_mov_b32_e32 v27, v2
	v_mov_b32_e32 v28, v2
	v_mov_b32_e32 v29, v2
	v_mov_b32_e32 v30, v2
	v_mov_b32_e32 v31, v2
	v_mov_b32_e32 v32, v2
	v_mov_b32_e32 v33, v2
	v_mov_b32_e32 v50, v2
	v_mov_b32_e32 v51, v2
	v_mov_b32_e32 v52, v2
	v_mov_b32_e32 v53, v2
	v_mov_b32_e32 v54, v2
	v_mov_b32_e32 v55, v2
	v_mov_b32_e32 v56, v2
	v_mov_b32_e32 v57, v2
	v_mov_b32_e32 v74, v2
	v_mov_b32_e32 v75, v2
	v_mov_b32_e32 v76, v2
	v_mov_b32_e32 v77, v2
	v_mov_b32_e32 v78, v2
	v_mov_b32_e32 v79, v2
	v_mov_b32_e32 v80, v2
	v_mov_b32_e32 v81, v2
	v_mov_b32_e32 v82, v2
	v_mov_b32_e32 v83, v2
	v_mov_b32_e32 v84, v2
	v_mov_b32_e32 v85, v2
	v_mov_b32_e32 v86, v2
	v_mov_b32_e32 v87, v2
	v_mov_b32_e32 v88, v2
	v_mov_b32_e32 v89, v2
	v_mov_b32_e32 v100, v2
	v_mov_b32_e32 v101, v2
	v_mov_b32_e32 v102, v2
	v_mov_b32_e32 v103, v2
	v_mov_b32_e32 v104, v2
	v_mov_b32_e32 v105, v2
	v_mov_b32_e32 v106, v2
	v_mov_b32_e32 v107, v2
	v_mov_b32_e32 v116, v2
	v_mov_b32_e32 v117, v2
	v_mov_b32_e32 v118, v2
	v_mov_b32_e32 v119, v2
	v_mov_b32_e32 v120, v2
	v_mov_b32_e32 v121, v2
	v_mov_b32_e32 v122, v2
	v_mov_b32_e32 v123, v2
	v_mov_b32_e32 v132, v2
	v_mov_b32_e32 v133, v2
	v_mov_b32_e32 v134, v2
	v_mov_b32_e32 v135, v2
	v_mov_b32_e32 v136, v2
	v_mov_b32_e32 v137, v2
	v_mov_b32_e32 v138, v2
	v_mov_b32_e32 v139, v2
	v_mov_b32_e32 v90, v2
	v_mov_b32_e32 v91, v2
	v_mov_b32_e32 v92, v2
	v_mov_b32_e32 v93, v2
	v_mov_b32_e32 v94, v2
	v_mov_b32_e32 v95, v2
	v_mov_b32_e32 v96, v2
	v_mov_b32_e32 v97, v2
	v_mov_b32_e32 v108, v2
	v_mov_b32_e32 v109, v2
	v_mov_b32_e32 v110, v2
	v_mov_b32_e32 v111, v2
	v_mov_b32_e32 v112, v2
	v_mov_b32_e32 v113, v2
	v_mov_b32_e32 v114, v2
	v_mov_b32_e32 v115, v2
	v_mov_b32_e32 v124, v2
	v_mov_b32_e32 v125, v2
	v_mov_b32_e32 v126, v2
	v_mov_b32_e32 v127, v2
	v_mov_b32_e32 v128, v2
	v_mov_b32_e32 v129, v2
	v_mov_b32_e32 v130, v2
	v_mov_b32_e32 v131, v2
	v_mov_b32_e32 v140, v2
	v_mov_b32_e32 v141, v2
	v_mov_b32_e32 v142, v2
	v_mov_b32_e32 v143, v2
	v_mov_b32_e32 v144, v2
	v_mov_b32_e32 v145, v2
	v_mov_b32_e32 v146, v2
	v_mov_b32_e32 v147, v2
	s_waitcnt vmcnt(8)
